# P9 epilogue: the early wave half's alignment barrier moved behind its round-0 SwiGLU math (overlaps the late half's last MFMA segment)
# baseline (speedup 1.0000x reference)
; #define LAS __attribute__((address_space(3)))
; __device__ __forceinline__ unsigned pk4_fp8(float a, float b, float c, float d) { int w = 0; w = __builtin_amdgcn_cvt_pk_fp8_f32(a, b, w, false); w = __builtin_amdgcn_cvt_pk_fp8_f32(c, d, w, true); return (unsigned)w; }
;     __device__ __forceinline__ void operator()(const f32x4 (&acc)[2][2][4][2], const Unit& u, int wr, int wc, int fr, int fq) const {
;         const int e = u.pn / npn, pnl = u.pn - e * npn; const int tid = threadIdx.x;
;         const int col0 = pnl * BM + wc * 32 + 8 * fq;
;         f32x4 bv[2][2];
; #pragma unroll
;         for (int bj = 0; bj < 2; ++bj)
; #pragma unroll
;             for (int n = 0; n < 2; ++n) bv[bj][n] = *(const f32x4*)(bias + (size_t)e * bias_ld + col0 + bj * HALF + 4 * n);
;         LAS unsigned char* wp = stg + (16 * wr + fr) * STG8_PITCH + 16 * wc + 4 * fq;
;         const int rr = (tid >> 3) & 31, cc = tid & 7, ms = tid >> 8;
;         const LAS unsigned char* rp = stg + rr * STG8_PITCH + cc * 16;
;         unsigned char* gp = O + (size_t)(u.pm * BM + 64 * (rr >> 4) + (rr & 15)) * ldc + pnl * (BM / 2) + cc * 16;
; #pragma unroll
;         for (int ai = 0; ai < 2; ++ai) {
; #pragma unroll
;             for (int m = 0; m < 4; ++m)
; #pragma unroll
;                 for (int bj = 0; bj < 2; ++bj) { const f32x4 v0 = acc[ai][bj][m][0] * scale + bv[bj][0], v1 = acc[ai][bj][m][1] * scale + bv[bj][1];
;                     *(LAS unsigned*)(wp + m * (32 * STG8_PITCH) + 64 * bj) = pk4_fp8(swiglu1(v0[0], v0[1]), swiglu1(v0[2], v0[3]), swiglu1(v1[0], v1[1]), swiglu1(v1[2], v1[3])); }
.LBB0_1010:
	s_cmp_eq_u32 s42, s46
	s_cselect_b32 s55, s23, s19
	s_ashr_i32 s2, s23, 31
	s_lshr_b32 s2, s2, 28
	s_add_i32 s3, s23, s2
	s_and_b32 s3, s3, -16
	s_sub_i32 s23, s23, s3
	s_ashr_i32 s2, s55, 31
	s_lshr_b32 s2, s2, 28
	s_add_i32 s3, s55, s2
	s_ashr_i32 s2, s3, 4
	s_and_b32 s3, s3, -16
	s_sub_i32 s54, s55, s3
	s_ashr_i32 s3, s2, 31
	s_lshl_b64 s[2:3], s[2:3], 14
	v_readlane_b32 s52, v254, 0
	v_lshl_or_b32 v2, s54, 8, v200
	v_readlane_b32 s53, v254, 1
	s_add_u32 s2, s52, s2
	s_addc_u32 s3, s53, s3
	v_ashrrev_i32_e32 v3, 31, v2
	s_nop 15
	s_nop 15
	v_lshl_add_u64 v[2:3], v[2:3], 2, s[2:3]
	global_load_dwordx4 v[208:211], v[2:3], off
	global_load_dwordx4 v[212:215], v[2:3], off offset:16
	global_load_dwordx4 v[216:219], v[2:3], off offset:512
	global_load_dwordx4 v[220:223], v[2:3], off offset:528
	v_lshl_or_b32 v18, s22, 8, v201
	v_ashrrev_i32_e32 v19, 31, v18
	v_lshlrev_b64 v[18:19], 11, v[18:19]
	s_lshl_b32 s22, s23, 7
	v_lshl_add_u64 v[18:19], s[8:9], 0, v[18:19]
	s_ashr_i32 s23, s22, 31
	v_lshl_add_u64 v[18:19], v[18:19], 0, s[22:23]
	v_lshl_add_u64 v[18:19], v[18:19], 0, v[170:171]
	s_cmp_eq_u32 s42, s46
	s_mov_b64 s[2:3], -1
	v_readlane_b32 s54, v254, 2
	v_readlane_b32 s55, v254, 3
	v_readlane_b32 s56, v254, 4
	v_readlane_b32 s57, v254, 5
	v_readlane_b32 s58, v254, 6
	v_readlane_b32 s59, v254, 7
	v_add_u32_e32 v22, 0x1000, v202
	v_add_u32_e32 v23, 0x2400, v202
	v_add_u32_e32 v24, 0x3400, v202
	v_min_f32_e32 v158, 0x43e00000, v158
	v_min_f32_e32 v160, 0x43e00000, v160
	v_min_f32_e32 v154, 0x43e00000, v154
	v_min_f32_e32 v156, 0x43e00000, v156
	v_mul_f32_e32 v2, 0xbd1d265f, v158
	v_mul_f32_e32 v3, 0xbd1d265f, v160
	v_mul_f32_e32 v4, 0xbd1d265f, v154
	v_mul_f32_e32 v5, 0xbd1d265f, v156
	v_exp_f32_e32 v2, v2
	v_exp_f32_e32 v3, v3
	v_exp_f32_e32 v4, v4
	v_exp_f32_e32 v5, v5
	v_fma_f32 v2, v2, v246, v246
	v_fma_f32 v3, v3, v246, v246
	v_fma_f32 v4, v4, v246, v246
	v_fma_f32 v5, v5, v246, v246
	v_rcp_f32_e32 v2, v2
	v_rcp_f32_e32 v3, v3
	v_rcp_f32_e32 v4, v4
	v_rcp_f32_e32 v5, v5
	v_med3_f32 v159, v159, s47, v204
	v_med3_f32 v161, v161, s47, v204
	v_med3_f32 v155, v155, s47, v204
	v_med3_f32 v157, v157, s47, v204
	v_mul_f32_e32 v158, v158, v2
	v_mul_f32_e32 v160, v160, v3
	v_mul_f32_e32 v154, v154, v4
	v_mul_f32_e32 v156, v156, v5
	v_mul_f32_e32 v158, v158, v159
	v_mul_f32_e32 v160, v160, v161
	v_mul_f32_e32 v154, v154, v155
	v_mul_f32_e32 v156, v156, v157
	v_cvt_pk_fp8_f32 v6, v158, v160
	v_cvt_pk_fp8_f32 v6, v154, v156 op_sel:[0,0,1]
	v_min_f32_e32 v150, 0x43e00000, v150
	v_min_f32_e32 v152, 0x43e00000, v152
	v_min_f32_e32 v146, 0x43e00000, v146
	v_min_f32_e32 v148, 0x43e00000, v148
	v_mul_f32_e32 v2, 0xbd1d265f, v150
	v_mul_f32_e32 v3, 0xbd1d265f, v152
	v_mul_f32_e32 v4, 0xbd1d265f, v146
	v_mul_f32_e32 v5, 0xbd1d265f, v148
	v_exp_f32_e32 v2, v2
	v_exp_f32_e32 v3, v3
	v_exp_f32_e32 v4, v4
	v_exp_f32_e32 v5, v5
	v_fma_f32 v2, v2, v246, v246
	v_fma_f32 v3, v3, v246, v246
	v_fma_f32 v4, v4, v246, v246
	v_fma_f32 v5, v5, v246, v246
	v_rcp_f32_e32 v2, v2
	v_rcp_f32_e32 v3, v3
	v_rcp_f32_e32 v4, v4
	v_rcp_f32_e32 v5, v5
	v_med3_f32 v151, v151, s47, v204
	v_med3_f32 v153, v153, s47, v204
	v_med3_f32 v147, v147, s47, v204
	v_med3_f32 v149, v149, s47, v204
	v_mul_f32_e32 v150, v150, v2
	v_mul_f32_e32 v152, v152, v3
	v_mul_f32_e32 v146, v146, v4
	v_mul_f32_e32 v148, v148, v5
	v_mul_f32_e32 v150, v150, v151
	v_mul_f32_e32 v152, v152, v153
	v_mul_f32_e32 v146, v146, v147
	v_mul_f32_e32 v148, v148, v149
	v_cvt_pk_fp8_f32 v7, v150, v152
	v_cvt_pk_fp8_f32 v7, v146, v148 op_sel:[0,0,1]
	v_min_f32_e32 v142, 0x43e00000, v142
	v_min_f32_e32 v144, 0x43e00000, v144
	v_min_f32_e32 v138, 0x43e00000, v138
	v_min_f32_e32 v140, 0x43e00000, v140
	v_mul_f32_e32 v2, 0xbd1d265f, v142
	v_mul_f32_e32 v3, 0xbd1d265f, v144
	v_mul_f32_e32 v4, 0xbd1d265f, v138
	v_mul_f32_e32 v5, 0xbd1d265f, v140
	v_exp_f32_e32 v2, v2
	v_exp_f32_e32 v3, v3
	v_exp_f32_e32 v4, v4
	v_exp_f32_e32 v5, v5
	v_fma_f32 v2, v2, v246, v246
	v_fma_f32 v3, v3, v246, v246
	v_fma_f32 v4, v4, v246, v246
	v_fma_f32 v5, v5, v246, v246
	v_rcp_f32_e32 v2, v2
	v_rcp_f32_e32 v3, v3
	v_rcp_f32_e32 v4, v4
	v_rcp_f32_e32 v5, v5
	v_med3_f32 v143, v143, s47, v204
	v_med3_f32 v145, v145, s47, v204
	v_med3_f32 v139, v139, s47, v204
	v_med3_f32 v141, v141, s47, v204
	v_mul_f32_e32 v142, v142, v2
	v_mul_f32_e32 v144, v144, v3
	v_mul_f32_e32 v138, v138, v4
	v_mul_f32_e32 v140, v140, v5
	v_mul_f32_e32 v142, v142, v143
	v_mul_f32_e32 v144, v144, v145
	v_mul_f32_e32 v138, v138, v139
	v_mul_f32_e32 v140, v140, v141
	v_cvt_pk_fp8_f32 v8, v142, v144
	v_cvt_pk_fp8_f32 v8, v138, v140 op_sel:[0,0,1]
	v_min_f32_e32 v134, 0x43e00000, v134
	v_min_f32_e32 v136, 0x43e00000, v136
	v_min_f32_e32 v130, 0x43e00000, v130
	v_min_f32_e32 v132, 0x43e00000, v132
	v_mul_f32_e32 v2, 0xbd1d265f, v134
	v_mul_f32_e32 v3, 0xbd1d265f, v136
	v_mul_f32_e32 v4, 0xbd1d265f, v130
	v_mul_f32_e32 v5, 0xbd1d265f, v132
	v_exp_f32_e32 v2, v2
	v_exp_f32_e32 v3, v3
	v_exp_f32_e32 v4, v4
	v_exp_f32_e32 v5, v5
	v_fma_f32 v2, v2, v246, v246
	v_fma_f32 v3, v3, v246, v246
	v_fma_f32 v4, v4, v246, v246
	v_fma_f32 v5, v5, v246, v246
	v_rcp_f32_e32 v2, v2
	v_rcp_f32_e32 v3, v3
	v_rcp_f32_e32 v4, v4
	v_rcp_f32_e32 v5, v5
	v_med3_f32 v135, v135, s47, v204
	v_med3_f32 v137, v137, s47, v204
	v_med3_f32 v131, v131, s47, v204
	v_med3_f32 v133, v133, s47, v204
	v_mul_f32_e32 v134, v134, v2
	v_mul_f32_e32 v136, v136, v3
	v_mul_f32_e32 v130, v130, v4
	v_mul_f32_e32 v132, v132, v5
	v_mul_f32_e32 v134, v134, v135
	v_mul_f32_e32 v136, v136, v137
	v_mul_f32_e32 v130, v130, v131
	v_mul_f32_e32 v132, v132, v133
	v_cvt_pk_fp8_f32 v9, v134, v136
	v_cvt_pk_fp8_f32 v9, v130, v132 op_sel:[0,0,1]
; #define LAS __attribute__((address_space(3)))
; __device__ __forceinline__ unsigned pk4_fp8(float a, float b, float c, float d) { int w = 0; w = __builtin_amdgcn_cvt_pk_fp8_f32(a, b, w, false); w = __builtin_amdgcn_cvt_pk_fp8_f32(c, d, w, true); return (unsigned)w; }
;     __device__ __forceinline__ void operator()(const f32x4 (&acc)[2][2][4][2], const Unit& u, int wr, int wc, int fr, int fq) const {
;     ...
; #pragma unroll
;             for (int m = 0; m < 4; ++m)
; #pragma unroll
;                 for (int bj = 0; bj < 2; ++bj) { const f32x4 v0 = acc[ai][bj][m][0] * scale + bv[bj][0], v1 = acc[ai][bj][m][1] * scale + bv[bj][1];
;                     *(LAS unsigned*)(wp + m * (32 * STG8_PITCH) + 64 * bj) = pk4_fp8(swiglu1(v0[0], v0[1]), swiglu1(v0[2], v0[3]), swiglu1(v1[0], v1[1]), swiglu1(v1[2], v1[3])); }
	v_min_f32_e32 v126, 0x43e00000, v126
	v_min_f32_e32 v128, 0x43e00000, v128
	v_min_f32_e32 v122, 0x43e00000, v122
	v_min_f32_e32 v124, 0x43e00000, v124
	v_mul_f32_e32 v2, 0xbd1d265f, v126
	v_mul_f32_e32 v3, 0xbd1d265f, v128
	v_mul_f32_e32 v4, 0xbd1d265f, v122
	v_mul_f32_e32 v5, 0xbd1d265f, v124
	v_exp_f32_e32 v2, v2
	v_exp_f32_e32 v3, v3
	v_exp_f32_e32 v4, v4
	v_exp_f32_e32 v5, v5
	v_fma_f32 v2, v2, v246, v246
	v_fma_f32 v3, v3, v246, v246
	v_fma_f32 v4, v4, v246, v246
	v_fma_f32 v5, v5, v246, v246
	v_rcp_f32_e32 v2, v2
	v_rcp_f32_e32 v3, v3
	v_rcp_f32_e32 v4, v4
	v_rcp_f32_e32 v5, v5
	v_med3_f32 v127, v127, s47, v204
	v_med3_f32 v129, v129, s47, v204
	v_med3_f32 v123, v123, s47, v204
	v_med3_f32 v125, v125, s47, v204
	v_mul_f32_e32 v126, v126, v2
	v_mul_f32_e32 v128, v128, v3
	v_mul_f32_e32 v122, v122, v4
	v_mul_f32_e32 v124, v124, v5
	v_mul_f32_e32 v126, v126, v127
	v_mul_f32_e32 v128, v128, v129
	v_mul_f32_e32 v122, v122, v123
	v_mul_f32_e32 v124, v124, v125
	v_cvt_pk_fp8_f32 v10, v126, v128
	v_cvt_pk_fp8_f32 v10, v122, v124 op_sel:[0,0,1]
	v_min_f32_e32 v118, 0x43e00000, v118
	v_min_f32_e32 v120, 0x43e00000, v120
	v_min_f32_e32 v114, 0x43e00000, v114
	v_min_f32_e32 v116, 0x43e00000, v116
	v_mul_f32_e32 v2, 0xbd1d265f, v118
	v_mul_f32_e32 v3, 0xbd1d265f, v120
	v_mul_f32_e32 v4, 0xbd1d265f, v114
	v_mul_f32_e32 v5, 0xbd1d265f, v116
	v_exp_f32_e32 v2, v2
	v_exp_f32_e32 v3, v3
	v_exp_f32_e32 v4, v4
	v_exp_f32_e32 v5, v5
	v_fma_f32 v2, v2, v246, v246
	v_fma_f32 v3, v3, v246, v246
	v_fma_f32 v4, v4, v246, v246
	v_fma_f32 v5, v5, v246, v246
	v_rcp_f32_e32 v2, v2
	v_rcp_f32_e32 v3, v3
	v_rcp_f32_e32 v4, v4
	v_rcp_f32_e32 v5, v5
	v_med3_f32 v119, v119, s47, v204
	v_med3_f32 v121, v121, s47, v204
	v_med3_f32 v115, v115, s47, v204
	v_med3_f32 v117, v117, s47, v204
	v_mul_f32_e32 v118, v118, v2
	v_mul_f32_e32 v120, v120, v3
	v_mul_f32_e32 v114, v114, v4
	v_mul_f32_e32 v116, v116, v5
	v_mul_f32_e32 v118, v118, v119
	v_mul_f32_e32 v120, v120, v121
	v_mul_f32_e32 v114, v114, v115
	v_mul_f32_e32 v116, v116, v117
	v_cvt_pk_fp8_f32 v11, v118, v120
	v_cvt_pk_fp8_f32 v11, v114, v116 op_sel:[0,0,1]
	v_min_f32_e32 v110, 0x43e00000, v110
	v_min_f32_e32 v112, 0x43e00000, v112
	v_min_f32_e32 v106, 0x43e00000, v106
	v_min_f32_e32 v108, 0x43e00000, v108
	v_mul_f32_e32 v2, 0xbd1d265f, v110
	v_mul_f32_e32 v3, 0xbd1d265f, v112
	v_mul_f32_e32 v4, 0xbd1d265f, v106
	v_mul_f32_e32 v5, 0xbd1d265f, v108
	v_exp_f32_e32 v2, v2
	v_exp_f32_e32 v3, v3
	v_exp_f32_e32 v4, v4
	v_exp_f32_e32 v5, v5
	v_fma_f32 v2, v2, v246, v246
	v_fma_f32 v3, v3, v246, v246
	v_fma_f32 v4, v4, v246, v246
	v_fma_f32 v5, v5, v246, v246
	v_rcp_f32_e32 v2, v2
	v_rcp_f32_e32 v3, v3
	v_rcp_f32_e32 v4, v4
	v_rcp_f32_e32 v5, v5
	v_med3_f32 v111, v111, s47, v204
	v_med3_f32 v113, v113, s47, v204
	v_med3_f32 v107, v107, s47, v204
	v_med3_f32 v109, v109, s47, v204
	v_mul_f32_e32 v110, v110, v2
	v_mul_f32_e32 v112, v112, v3
	v_mul_f32_e32 v106, v106, v4
	v_mul_f32_e32 v108, v108, v5
	v_mul_f32_e32 v110, v110, v111
	v_mul_f32_e32 v112, v112, v113
	v_mul_f32_e32 v106, v106, v107
	v_mul_f32_e32 v108, v108, v109
	v_cvt_pk_fp8_f32 v12, v110, v112
	v_cvt_pk_fp8_f32 v12, v106, v108 op_sel:[0,0,1]
	v_min_f32_e32 v102, 0x43e00000, v102
	v_min_f32_e32 v104, 0x43e00000, v104
	v_min_f32_e32 v98, 0x43e00000, v98
	v_min_f32_e32 v100, 0x43e00000, v100
	v_mul_f32_e32 v2, 0xbd1d265f, v102
	v_mul_f32_e32 v3, 0xbd1d265f, v104
	v_mul_f32_e32 v4, 0xbd1d265f, v98
	v_mul_f32_e32 v5, 0xbd1d265f, v100
	v_exp_f32_e32 v2, v2
	v_exp_f32_e32 v3, v3
	v_exp_f32_e32 v4, v4
	v_exp_f32_e32 v5, v5
	v_fma_f32 v2, v2, v246, v246
	v_fma_f32 v3, v3, v246, v246
	v_fma_f32 v4, v4, v246, v246
	v_fma_f32 v5, v5, v246, v246
	v_rcp_f32_e32 v2, v2
	v_rcp_f32_e32 v3, v3
	v_rcp_f32_e32 v4, v4
	v_rcp_f32_e32 v5, v5
	v_med3_f32 v103, v103, s47, v204
	v_med3_f32 v105, v105, s47, v204
	v_med3_f32 v99, v99, s47, v204
	v_med3_f32 v101, v101, s47, v204
	v_mul_f32_e32 v102, v102, v2
	v_mul_f32_e32 v104, v104, v3
	v_mul_f32_e32 v98, v98, v4
	v_mul_f32_e32 v100, v100, v5
	v_mul_f32_e32 v102, v102, v103
	v_mul_f32_e32 v104, v104, v105
	v_mul_f32_e32 v98, v98, v99
	v_mul_f32_e32 v100, v100, v101
	v_cvt_pk_fp8_f32 v13, v102, v104
	v_cvt_pk_fp8_f32 v13, v98, v100 op_sel:[0,0,1]
	s_and_b64 vcc, exec, s[12:13]
	s_cbranch_vccz .Lp9_noalign
	s_barrier
; #define LAS __attribute__((address_space(3)))
; __device__ __forceinline__ unsigned pk4_fp8(float a, float b, float c, float d) { int w = 0; w = __builtin_amdgcn_cvt_pk_fp8_f32(a, b, w, false); w = __builtin_amdgcn_cvt_pk_fp8_f32(c, d, w, true); return (unsigned)w; }
; __device__ __forceinline__ float swiglu1(float g, float l) {
;     g = fminf(g, 7.0f); l = fminf(fmaxf(l, -7.0f), 7.0f);
;     const float s = __builtin_amdgcn_rcpf(1.0f + __expf(-1.702f * g));
;     return g * s * (l + 1.0f);
; }
;     __device__ __forceinline__ void operator()(const f32x4 (&acc)[2][2][4][2], const Unit& u, int wr, int wc, int fr, int fq) const {
;     ...
; #pragma unroll
;             for (int m = 0; m < 4; ++m)
; #pragma unroll
;                 for (int bj = 0; bj < 2; ++bj) { const f32x4 v0 = acc[ai][bj][m][0] * scale + bv[bj][0], v1 = acc[ai][bj][m][1] * scale + bv[bj][1];
;                     *(LAS unsigned*)(wp + m * (32 * STG8_PITCH) + 64 * bj) = pk4_fp8(swiglu1(v0[0], v0[1]), swiglu1(v0[2], v0[3]), swiglu1(v1[0], v1[1]), swiglu1(v1[2], v1[3])); }
.Lp9_noalign:
	s_cmp_eq_u32 s42, s46
	v_min_f32_e32 v94, 0x43e00000, v94
	v_min_f32_e32 v96, 0x43e00000, v96
	v_min_f32_e32 v90, 0x43e00000, v90
	v_min_f32_e32 v92, 0x43e00000, v92
	v_mul_f32_e32 v2, 0xbd1d265f, v94
	v_mul_f32_e32 v3, 0xbd1d265f, v96
	v_mul_f32_e32 v4, 0xbd1d265f, v90
	v_mul_f32_e32 v5, 0xbd1d265f, v92
	v_exp_f32_e32 v2, v2
	v_exp_f32_e32 v3, v3
	v_exp_f32_e32 v4, v4
	v_exp_f32_e32 v5, v5
	v_fma_f32 v2, v2, v246, v246
	v_fma_f32 v3, v3, v246, v246
	v_fma_f32 v4, v4, v246, v246
	v_fma_f32 v5, v5, v246, v246
	v_rcp_f32_e32 v2, v2
	v_rcp_f32_e32 v3, v3
	v_rcp_f32_e32 v4, v4
	v_rcp_f32_e32 v5, v5
	v_med3_f32 v95, v95, s47, v204
	v_med3_f32 v97, v97, s47, v204
	v_med3_f32 v91, v91, s47, v204
	v_med3_f32 v93, v93, s47, v204
	v_mul_f32_e32 v94, v94, v2
	v_mul_f32_e32 v96, v96, v3
	v_mul_f32_e32 v90, v90, v4
	v_mul_f32_e32 v92, v92, v5
	v_mul_f32_e32 v94, v94, v95
	v_mul_f32_e32 v96, v96, v97
	v_mul_f32_e32 v90, v90, v91
	v_mul_f32_e32 v92, v92, v93
	v_cvt_pk_fp8_f32 v26, v94, v96
	v_cvt_pk_fp8_f32 v26, v90, v92 op_sel:[0,0,1]
	v_min_f32_e32 v86, 0x43e00000, v86
	v_min_f32_e32 v88, 0x43e00000, v88
	v_min_f32_e32 v82, 0x43e00000, v82
	v_min_f32_e32 v84, 0x43e00000, v84
	v_mul_f32_e32 v2, 0xbd1d265f, v86
	v_mul_f32_e32 v3, 0xbd1d265f, v88
	v_mul_f32_e32 v4, 0xbd1d265f, v82
	v_mul_f32_e32 v5, 0xbd1d265f, v84
	v_exp_f32_e32 v2, v2
	v_exp_f32_e32 v3, v3
	v_exp_f32_e32 v4, v4
	v_exp_f32_e32 v5, v5
	v_fma_f32 v2, v2, v246, v246
	v_fma_f32 v3, v3, v246, v246
	v_fma_f32 v4, v4, v246, v246
	v_fma_f32 v5, v5, v246, v246
	v_rcp_f32_e32 v2, v2
	v_rcp_f32_e32 v3, v3
	v_rcp_f32_e32 v4, v4
	v_rcp_f32_e32 v5, v5
	v_med3_f32 v87, v87, s47, v204
	v_med3_f32 v89, v89, s47, v204
	v_med3_f32 v83, v83, s47, v204
	v_med3_f32 v85, v85, s47, v204
	v_mul_f32_e32 v86, v86, v2
	v_mul_f32_e32 v88, v88, v3
	v_mul_f32_e32 v82, v82, v4
	v_mul_f32_e32 v84, v84, v5
	v_mul_f32_e32 v86, v86, v87
	v_mul_f32_e32 v88, v88, v89
	v_mul_f32_e32 v82, v82, v83
	v_mul_f32_e32 v84, v84, v85
	v_cvt_pk_fp8_f32 v27, v86, v88
	v_cvt_pk_fp8_f32 v27, v82, v84 op_sel:[0,0,1]
	v_min_f32_e32 v78, 0x43e00000, v78
	v_min_f32_e32 v80, 0x43e00000, v80
	v_min_f32_e32 v74, 0x43e00000, v74
	v_min_f32_e32 v76, 0x43e00000, v76
	v_mul_f32_e32 v2, 0xbd1d265f, v78
	v_mul_f32_e32 v3, 0xbd1d265f, v80
	v_mul_f32_e32 v4, 0xbd1d265f, v74
	v_mul_f32_e32 v5, 0xbd1d265f, v76
	v_exp_f32_e32 v2, v2
	v_exp_f32_e32 v3, v3
	v_exp_f32_e32 v4, v4
	v_exp_f32_e32 v5, v5
	v_fma_f32 v2, v2, v246, v246
	v_fma_f32 v3, v3, v246, v246
	v_fma_f32 v4, v4, v246, v246
	v_fma_f32 v5, v5, v246, v246
	v_rcp_f32_e32 v2, v2
	v_rcp_f32_e32 v3, v3
	v_rcp_f32_e32 v4, v4
	v_rcp_f32_e32 v5, v5
	v_med3_f32 v79, v79, s47, v204
	v_med3_f32 v81, v81, s47, v204
	v_med3_f32 v75, v75, s47, v204
	v_med3_f32 v77, v77, s47, v204
	v_mul_f32_e32 v78, v78, v2
	v_mul_f32_e32 v80, v80, v3
	v_mul_f32_e32 v74, v74, v4
	v_mul_f32_e32 v76, v76, v5
	v_mul_f32_e32 v78, v78, v79
	v_mul_f32_e32 v80, v80, v81
	v_mul_f32_e32 v74, v74, v75
	v_mul_f32_e32 v76, v76, v77
	v_cvt_pk_fp8_f32 v28, v78, v80
	v_cvt_pk_fp8_f32 v28, v74, v76 op_sel:[0,0,1]
	v_min_f32_e32 v70, 0x43e00000, v70
	v_min_f32_e32 v72, 0x43e00000, v72
	v_min_f32_e32 v66, 0x43e00000, v66
	v_min_f32_e32 v68, 0x43e00000, v68
	v_mul_f32_e32 v2, 0xbd1d265f, v70
	v_mul_f32_e32 v3, 0xbd1d265f, v72
	v_mul_f32_e32 v4, 0xbd1d265f, v66
	v_mul_f32_e32 v5, 0xbd1d265f, v68
	v_exp_f32_e32 v2, v2
	v_exp_f32_e32 v3, v3
	v_exp_f32_e32 v4, v4
	v_exp_f32_e32 v5, v5
	v_fma_f32 v2, v2, v246, v246
	v_fma_f32 v3, v3, v246, v246
	v_fma_f32 v4, v4, v246, v246
	v_fma_f32 v5, v5, v246, v246
	v_rcp_f32_e32 v2, v2
	v_rcp_f32_e32 v3, v3
	v_rcp_f32_e32 v4, v4
	v_rcp_f32_e32 v5, v5
	v_med3_f32 v71, v71, s47, v204
	v_med3_f32 v73, v73, s47, v204
	v_med3_f32 v67, v67, s47, v204
	v_med3_f32 v69, v69, s47, v204
	v_mul_f32_e32 v70, v70, v2
	v_mul_f32_e32 v72, v72, v3
	v_mul_f32_e32 v66, v66, v4
	v_mul_f32_e32 v68, v68, v5
	v_mul_f32_e32 v70, v70, v71
	v_mul_f32_e32 v72, v72, v73
	v_mul_f32_e32 v66, v66, v67
	v_mul_f32_e32 v68, v68, v69
	v_cvt_pk_fp8_f32 v29, v70, v72
	v_cvt_pk_fp8_f32 v29, v66, v68 op_sel:[0,0,1]
	v_min_f32_e32 v58, 0x43e00000, v58
	v_min_f32_e32 v60, 0x43e00000, v60
	v_min_f32_e32 v50, 0x43e00000, v50
	v_min_f32_e32 v52, 0x43e00000, v52
	v_mul_f32_e32 v2, 0xbd1d265f, v58
	v_mul_f32_e32 v3, 0xbd1d265f, v60
	v_mul_f32_e32 v4, 0xbd1d265f, v50
	v_mul_f32_e32 v5, 0xbd1d265f, v52
	v_exp_f32_e32 v2, v2
	v_exp_f32_e32 v3, v3
	v_exp_f32_e32 v4, v4
	v_exp_f32_e32 v5, v5
	v_fma_f32 v2, v2, v246, v246
	v_fma_f32 v3, v3, v246, v246
	v_fma_f32 v4, v4, v246, v246
	v_fma_f32 v5, v5, v246, v246
	v_rcp_f32_e32 v2, v2
	v_rcp_f32_e32 v3, v3
	v_rcp_f32_e32 v4, v4
	v_rcp_f32_e32 v5, v5
	v_med3_f32 v59, v59, s47, v204
	v_med3_f32 v61, v61, s47, v204
	v_med3_f32 v51, v51, s47, v204
	v_med3_f32 v53, v53, s47, v204
	v_mul_f32_e32 v58, v58, v2
	v_mul_f32_e32 v60, v60, v3
	v_mul_f32_e32 v50, v50, v4
	v_mul_f32_e32 v52, v52, v5
	v_mul_f32_e32 v58, v58, v59
	v_mul_f32_e32 v60, v60, v61
	v_mul_f32_e32 v50, v50, v51
	v_mul_f32_e32 v52, v52, v53
; #define LAS __attribute__((address_space(3)))
; __device__ __forceinline__ unsigned pk4_fp8(float a, float b, float c, float d) { int w = 0; w = __builtin_amdgcn_cvt_pk_fp8_f32(a, b, w, false); w = __builtin_amdgcn_cvt_pk_fp8_f32(c, d, w, true); return (unsigned)w; }
;     __device__ __forceinline__ void operator()(const f32x4 (&acc)[2][2][4][2], const Unit& u, int wr, int wc, int fr, int fq) const {
;     ...
; #pragma unroll
;             for (int m = 0; m < 4; ++m)
; #pragma unroll
;                 for (int bj = 0; bj < 2; ++bj) { const f32x4 v0 = acc[ai][bj][m][0] * scale + bv[bj][0], v1 = acc[ai][bj][m][1] * scale + bv[bj][1];
;                     *(LAS unsigned*)(wp + m * (32 * STG8_PITCH) + 64 * bj) = pk4_fp8(swiglu1(v0[0], v0[1]), swiglu1(v0[2], v0[3]), swiglu1(v1[0], v1[1]), swiglu1(v1[2], v1[3])); }
;             asm volatile("s_waitcnt lgkmcnt(0)" ::: "memory"); __builtin_amdgcn_s_barrier(); asm volatile("" ::: "memory");
; #pragma unroll
;             for (int k2 = 0; k2 < 2; ++k2) { const int m = ms + 2 * k2;
;                 *(u32x4*)(gp + (size_t)(ai * HALF + m * 16) * ldc) = *(const LAS u32x4*)(rp + m * (32 * STG8_PITCH)); }
;             asm volatile("s_waitcnt lgkmcnt(0)" ::: "memory"); __builtin_amdgcn_s_barrier(); asm volatile("" ::: "memory");
;         }
	v_cvt_pk_fp8_f32 v30, v58, v60
	v_cvt_pk_fp8_f32 v30, v50, v52 op_sel:[0,0,1]
	v_min_f32_e32 v62, 0x43e00000, v62
	v_min_f32_e32 v64, 0x43e00000, v64
	v_min_f32_e32 v54, 0x43e00000, v54
	v_min_f32_e32 v56, 0x43e00000, v56
	v_mul_f32_e32 v2, 0xbd1d265f, v62
	v_mul_f32_e32 v3, 0xbd1d265f, v64
	v_mul_f32_e32 v4, 0xbd1d265f, v54
	v_mul_f32_e32 v5, 0xbd1d265f, v56
	v_exp_f32_e32 v2, v2
	v_exp_f32_e32 v3, v3
	v_exp_f32_e32 v4, v4
	v_exp_f32_e32 v5, v5
	v_fma_f32 v2, v2, v246, v246
	v_fma_f32 v3, v3, v246, v246
	v_fma_f32 v4, v4, v246, v246
	v_fma_f32 v5, v5, v246, v246
	v_rcp_f32_e32 v2, v2
	v_rcp_f32_e32 v3, v3
	v_rcp_f32_e32 v4, v4
	v_rcp_f32_e32 v5, v5
	v_med3_f32 v63, v63, s47, v204
	v_med3_f32 v65, v65, s47, v204
	v_med3_f32 v55, v55, s47, v204
	v_med3_f32 v57, v57, s47, v204
	v_mul_f32_e32 v62, v62, v2
	v_mul_f32_e32 v64, v64, v3
	v_mul_f32_e32 v54, v54, v4
	v_mul_f32_e32 v56, v56, v5
	v_mul_f32_e32 v62, v62, v63
	v_mul_f32_e32 v64, v64, v65
	v_mul_f32_e32 v54, v54, v55
	v_mul_f32_e32 v56, v56, v57
	v_cvt_pk_fp8_f32 v31, v62, v64
	v_cvt_pk_fp8_f32 v31, v54, v56 op_sel:[0,0,1]
	v_min_f32_e32 v38, 0x43e00000, v38
	v_min_f32_e32 v40, 0x43e00000, v40
	v_min_f32_e32 v34, 0x43e00000, v34
	v_min_f32_e32 v36, 0x43e00000, v36
	v_mul_f32_e32 v2, 0xbd1d265f, v38
	v_mul_f32_e32 v3, 0xbd1d265f, v40
	v_mul_f32_e32 v4, 0xbd1d265f, v34
	v_mul_f32_e32 v5, 0xbd1d265f, v36
	v_exp_f32_e32 v2, v2
	v_exp_f32_e32 v3, v3
	v_exp_f32_e32 v4, v4
	v_exp_f32_e32 v5, v5
	v_fma_f32 v2, v2, v246, v246
	v_fma_f32 v3, v3, v246, v246
	v_fma_f32 v4, v4, v246, v246
	v_fma_f32 v5, v5, v246, v246
	v_rcp_f32_e32 v2, v2
	v_rcp_f32_e32 v3, v3
	v_rcp_f32_e32 v4, v4
	v_rcp_f32_e32 v5, v5
	v_med3_f32 v39, v39, s47, v204
	v_med3_f32 v41, v41, s47, v204
	v_med3_f32 v35, v35, s47, v204
	v_med3_f32 v37, v37, s47, v204
	v_mul_f32_e32 v38, v38, v2
	v_mul_f32_e32 v40, v40, v3
	v_mul_f32_e32 v34, v34, v4
	v_mul_f32_e32 v36, v36, v5
	v_mul_f32_e32 v38, v38, v39
	v_mul_f32_e32 v40, v40, v41
	v_mul_f32_e32 v34, v34, v35
	v_mul_f32_e32 v36, v36, v37
	v_cvt_pk_fp8_f32 v32, v38, v40
	v_cvt_pk_fp8_f32 v32, v34, v36 op_sel:[0,0,1]
	v_min_f32_e32 v46, 0x43e00000, v46
	v_min_f32_e32 v48, 0x43e00000, v48
	v_min_f32_e32 v42, 0x43e00000, v42
	v_min_f32_e32 v44, 0x43e00000, v44
	v_mul_f32_e32 v2, 0xbd1d265f, v46
	v_mul_f32_e32 v3, 0xbd1d265f, v48
	v_mul_f32_e32 v4, 0xbd1d265f, v42
	v_mul_f32_e32 v5, 0xbd1d265f, v44
	v_exp_f32_e32 v2, v2
	v_exp_f32_e32 v3, v3
	v_exp_f32_e32 v4, v4
	v_exp_f32_e32 v5, v5
	v_fma_f32 v2, v2, v246, v246
	v_fma_f32 v3, v3, v246, v246
	v_fma_f32 v4, v4, v246, v246
	v_fma_f32 v5, v5, v246, v246
	v_rcp_f32_e32 v2, v2
	v_rcp_f32_e32 v3, v3
	v_rcp_f32_e32 v4, v4
	v_rcp_f32_e32 v5, v5
	v_med3_f32 v47, v47, s47, v204
	v_med3_f32 v49, v49, s47, v204
	v_med3_f32 v43, v43, s47, v204
	v_med3_f32 v45, v45, s47, v204
	v_mul_f32_e32 v46, v46, v2
	v_mul_f32_e32 v48, v48, v3
	v_mul_f32_e32 v42, v42, v4
	v_mul_f32_e32 v44, v44, v5
	v_mul_f32_e32 v46, v46, v47
	v_mul_f32_e32 v48, v48, v49
	v_mul_f32_e32 v42, v42, v43
	v_mul_f32_e32 v44, v44, v45
	v_cvt_pk_fp8_f32 v33, v46, v48
	v_cvt_pk_fp8_f32 v33, v42, v44 op_sel:[0,0,1]
	v_add_u32_e32 v14, 0xfffe7000, v202
	v_add_u32_e32 v15, 0xfffe8000, v202
	v_add_u32_e32 v16, 0xfffe9400, v202
	v_add_u32_e32 v17, 0xfffea400, v202
	ds_write2_b32 v202, v6, v7 offset1:16
	ds_write2_b32 v22, v8, v9 offset0:128 offset1:144
	ds_write2_b32 v23, v10, v11 offset1:16
	ds_write2_b32 v24, v12, v13 offset0:128 offset1:144
	ds_write2_b32 v14, v26, v27 offset1:16
	ds_write2_b32 v15, v28, v29 offset0:128 offset1:144
	ds_write2_b32 v16, v30, v31 offset1:16
	ds_write2_b32 v17, v32, v33 offset0:128 offset1:144
	s_waitcnt lgkmcnt(0)
	s_barrier
	v_add_u32_e32 v14, 0xfffe7000, v203
	ds_read_b128 v[26:29], v203
	ds_read_b128 v[30:33], v203 offset:9216
	ds_read_b128 v[2:5], v14
	ds_read_b128 v[6:9], v14 offset:9216
	v_lshl_add_u64 v[20:21], v[18:19], 0, v[172:173]
	v_lshl_add_u64 v[18:19], v[18:19], 0, v[174:175]
	v_add_co_u32_e32 v10, vcc, s48, v20
	s_nop 1
	v_addc_co_u32_e32 v11, vcc, 0, v21, vcc
	v_add_co_u32_e32 v12, vcc, 0x40000, v18
	s_nop 1
	v_addc_co_u32_e32 v13, vcc, 0, v19, vcc
	s_waitcnt lgkmcnt(3)
	global_store_dwordx4 v[20:21], v[26:29], off
	s_waitcnt lgkmcnt(2)
	global_store_dwordx4 v[18:19], v[30:33], off
	s_waitcnt lgkmcnt(1)
	global_store_dwordx4 v[10:11], v[2:5], off
	s_waitcnt lgkmcnt(0)
	global_store_dwordx4 v[12:13], v[6:9], off
	s_barrier
	s_waitcnt vmcnt(4)
	v_mul_f32_e32 v208, v247, v208
	v_fma_f32 v209, v209, v247, v247
	v_mul_f32_e32 v210, v247, v210
	v_fma_f32 v211, v211, v247, v247
	v_mul_f32_e32 v212, v247, v212
	v_fma_f32 v213, v213, v247, v247
	v_mul_f32_e32 v214, v247, v214
	v_fma_f32 v215, v215, v247, v247
	v_mul_f32_e32 v216, v247, v216
	v_fma_f32 v217, v217, v247, v247
	v_mul_f32_e32 v218, v247, v218
	v_fma_f32 v219, v219, v247, v247
	v_mul_f32_e32 v220, v247, v220
	v_fma_f32 v221, v221, v247, v247
	v_mul_f32_e32 v222, v247, v222
	v_fma_f32 v223, v223, v247, v247
	s_cbranch_scc1 .LBB0_993
	s_andn2_b64 vcc, exec, s[6:7]
	s_cbranch_vccnz .LBB0_992
	s_barrier
	s_branch .LBB0_992
